# s19b
# baseline (speedup 1.0000x reference)
_Z11attn_kernelILi4EEvPKfS1_S1_S1_S1_S1_PKcPf:
	s_load_dwordx2 s[24:25], s[0:1], 0x30
	s_load_dwordx8 s[8:15], s[0:1], 0x0
	s_load_dwordx4 s[16:19], s[0:1], 0x20
	v_lshrrev_b32_e32 v63, 6, v0
	v_and_b32_e32 v57, 15, v0
	v_bfe_u32 v1, v0, 4, 2
	v_lshrrev_b32_e32 v2, 2, v57
	v_mul_u32_u24_e32 v4, 3, v1
	v_mul_u32_u24_e32 v2, 3, v2
	v_mad_u32_u24 v4, v63, 12, v4
	v_mad_u32_u24 v2, v63, 12, v2
	v_lshlrev_b32_e32 v4, 2, v4
	v_lshlrev_b32_e32 v2, 2, v2
	v_and_b32_e32 v104, 63, v0
	v_lshlrev_b32_e32 v60, 5, v57
	v_lshlrev_b32_e32 v58, 3, v1
	v_add_u32_e32 v3, v60, v58
	v_lshrrev_b32_e32 v56, 4, v0
	v_lshlrev_b32_e32 v54, 4, v57
	v_mov_b32_e32 v59, 0
	s_movk_i32 s4, 0xe0
	v_cmp_gt_u32_e64 s[4:5], s4, v0
	s_lshl_b32 s26, s2, 8
	s_lshl_b32 s27, s2, 9
	s_mul_i32 s28, s2, 14
	s_add_u32 s26, s26, 0x164000
	s_add_u32 s27, s27, 0x80000
	s_add_u32 s20, s26, 0xc0
	v_min_u32_e32 v5, 2, v57
	v_lshlrev_b32_e32 v147, 6, v57
	v_lshlrev_b32_e32 v5, 2, v5
	v_add_u32_e32 v2, s26, v2
	v_add_u32_e32 v4, s26, v4
	v_add_u32_e32 v3, s27, v3
	v_mul_u32_u24_e32 v156, 0x140, v1
	s_movk_i32 s21, 0x500
	v_mad_u32_u24 v156, v63, s21, v156
	v_lshl_or_b32 v156, v57, 2, v156
	v_add_u32_e32 v156, 0x1c00, v156
	v_lshlrev_b32_e32 v157, 5, v56
	v_cmp_gt_u32_e32 vcc, 3, v57
	v_add_u32_e32 v158, 4, v57
	v_lshlrev_b32_e32 v159, 2, v57
	s_movk_i32 s21, 0x50
	v_cndmask_b32_e32 v158, 4, v158, vcc
	v_mad_u32_u24 v159, v56, s21, v159
	v_lshl_add_u32 v158, v158, 2, v157
	v_mul_u32_u24_e32 v250, 0x50, v56
	v_or_b32_e32 v250, 0x3800, v250
	v_lshl_add_u32 v251, v57, 1, v250
	v_mul_u32_u24_e32 v252, 0x50, v57
	v_lshl_add_u32 v252, v58, 1, v252
	v_lshlrev_b32_e32 v253, 2, v57
	v_and_b32_e32 v254, 0xc0, v0
	v_lshlrev_b32_e32 v255, 11, v1
	v_or3_b32 v253, v253, v254, v255
	v_add_u32_e32 v254, s28, v56
	v_lshl_add_u32 v254, v254, 9, v54
	v_lshl_or_b32 v255, v56, 9, v54
	s_waitcnt lgkmcnt(0)
	global_load_dwordx3 v[80:82], v2, s[24:25]
	global_load_dwordx3 v[84:86], v4, s[24:25]
	global_load_dwordx2 v[64:65], v3, s[24:25]
	s_load_dword s3, s[24:25], s20
	s_add_u32 s22, s24, 0x160000
	s_addc_u32 s23, s25, 0
	v_cndmask_b32_e64 v62, 13, v56, s[4:5]
	v_add_u32_e32 v3, s28, v62
	v_mad_u32_u24 v144, v3, 12, v5
	v_mad_u32_u24 v145, v3, 36, v5
	v_mad_u32_u24 v61, v56, 3, v57
	v_add_u32_e32 v62, 56, v61
	v_mul_u32_u24_e32 v146, 0x2493, v61
	v_mul_u32_u24_e32 v119, 0x2493, v62
	v_lshrrev_b32_e32 v146, 16, v146
	v_lshrrev_b32_e32 v119, 16, v119
	v_mul_u32_u24_e32 v146, 66, v146
	v_mul_u32_u24_e32 v119, 66, v119
	v_lshl_add_u32 v61, v61, 1, v146
	v_lshl_add_u32 v62, v62, 1, v119
	v_cmp_lt_u32_e32 vcc, 6, v56
	v_lshlrev_b32_e32 v119, 1, v56
	v_mov_b32_e32 v146, 0x42
	v_cndmask_b32_e32 v146, 0, v146, vcc
	v_add_u32_e32 v119, v119, v146
	v_lshl_or_b32 v147, v63, 10, v147
	v_lshl_or_b32 v147, v1, 4, v147
	v_or_b32_e32 v148, 0x1000, v147
	v_lshlrev_b32_e32 v149, 4, v104
	v_lshlrev_b32_e32 v150, 9, v3
	v_add_u32_e32 v150, v150, v54
	v_and_b32_e32 v87, 3, v57
	v_lshlrev_b32_e32 v87, 4, v87
	v_lshl_or_b32 v87, v1, 6, v87
	v_lshlrev_b32_e32 v88, 3, v57
	s_add_u32 s26, s24, 0x100000
	s_addc_u32 s27, s25, 0
	s_add_u32 s28, s24, 0x140000
	s_addc_u32 s29, s25, 0
	s_movk_i32 s6, 0x140
	v_cmp_gt_u32_e32 vcc, s6, v0
	v_lshlrev_b32_e32 v22, 2, v0
	v_mov_b32_e32 v23, 0
	s_and_saveexec_b64 s[6:7], vcc
	ds_write_b32 v22, v23 offset:14336
	s_or_b64 exec, exec, s[6:7]
	v_cmp_gt_u32_e32 vcc, 64, v0
	s_and_saveexec_b64 s[6:7], vcc
	ds_write_b32 v22, v23 offset:15360
	s_or_b64 exec, exec, s[6:7]
	v_mov_b32_e32 v45, 0xc9c35000
	s_mov_b32 s30, 0x3db8aa3b
	s_mov_b32 s31, 0x3db8aa3b
	v_mov_b32_e32 v121, 0x3fb8aa3b
	v_mov_b32_e32 v35, 0
	v_mov_b32_e32 v44, v45
	s_waitcnt lgkmcnt(0)
	s_bitcmp0_b32 s3, 1
	s_cselect_b64 s[20:21], -1, 0
	s_cbranch_scc1 .LBB1_16
	v_bfe_u32 v46, s3, v57, 1
	v_cmp_eq_u32_e32 vcc, 0, v46
	s_nop 1
	v_cndmask_b32_e32 v47, 0, v45, vcc
	v_cndmask_b32_e64 v55, 1.0, 0, vcc
	s_nop 0
	v_mov_b32_dpp v34, v47 row_newbcast:0 row_mask:0xf bank_mask:0xf bound_ctrl:1
	v_mov_b32_dpp v36, v47 row_newbcast:2 row_mask:0xf bank_mask:0xf bound_ctrl:1
	v_mov_b32_dpp v37, v47 row_newbcast:3 row_mask:0xf bank_mask:0xf bound_ctrl:1
	v_mov_b32_dpp v22, v47 row_newbcast:4 row_mask:0xf bank_mask:0xf bound_ctrl:1
	v_mov_b32_dpp v23, v47 row_newbcast:5 row_mask:0xf bank_mask:0xf bound_ctrl:1
	v_mov_b32_dpp v24, v47 row_newbcast:6 row_mask:0xf bank_mask:0xf bound_ctrl:1
	v_mov_b32_dpp v25, v47 row_newbcast:7 row_mask:0xf bank_mask:0xf bound_ctrl:1
	v_mov_b32_dpp v38, v47 row_newbcast:8 row_mask:0xf bank_mask:0xf bound_ctrl:1
	v_mov_b32_dpp v39, v47 row_newbcast:9 row_mask:0xf bank_mask:0xf bound_ctrl:1
	v_mov_b32_dpp v40, v47 row_newbcast:10 row_mask:0xf bank_mask:0xf bound_ctrl:1
	v_mov_b32_dpp v41, v47 row_newbcast:11 row_mask:0xf bank_mask:0xf bound_ctrl:1
	v_mov_b32_dpp v42, v47 row_newbcast:12 row_mask:0xf bank_mask:0xf bound_ctrl:1
	v_mov_b32_dpp v43, v47 row_newbcast:13 row_mask:0xf bank_mask:0xf bound_ctrl:1
	s_waitcnt vmcnt(1)
	v_lshl_add_u32 v72, v80, 9, v87
	v_lshl_add_u32 v73, v81, 9, v87
	v_lshl_add_u32 v74, v82, 9, v87
	global_load_dwordx4 v[50:53], v72, s[24:25]
	global_load_dwordx4 v[46:49], v72, s[24:25] offset:256
	global_load_dwordx4 v[14:17], v73, s[24:25]
	global_load_dwordx4 v[10:13], v73, s[24:25] offset:256
	global_load_dwordx4 v[6:9], v74, s[24:25]
	global_load_dwordx4 v[2:5], v74, s[24:25] offset:256
	v_lshl_add_u32 v75, v84, 8, v54
	v_lshl_add_u32 v78, v84, 7, v88
	v_lshl_add_u32 v76, v85, 8, v54
	v_lshl_add_u32 v79, v85, 7, v88
	v_lshl_add_u32 v77, v86, 8, v54
	v_lshl_add_u32 v80, v86, 7, v88
	global_load_dwordx4 v[30:33], v75, s[26:27]
	global_load_dwordx2 v[70:71], v78, s[28:29]
	global_load_dwordx4 v[26:29], v76, s[26:27]
	global_load_dwordx2 v[66:67], v79, s[28:29]
	global_load_dwordx4 v[18:21], v77, s[26:27]
	global_load_dwordx2 v[68:69], v80, s[28:29]
	global_load_dword v120, v144, s[12:13]
	global_load_dword v151, v144, s[14:15]
	global_load_dword v97, v145, s[10:11]
	global_load_dword v99, v145, s[10:11] offset:12
	global_load_dword v113, v145, s[10:11] offset:24
	global_load_dwordx4 v[124:127], v147, s[22:23]
	global_load_dwordx4 v[128:131], v148, s[22:23]
	s_mov_b32 exec_hi, 0
	global_load_dwordx4 v[132:135], v149, s[16:17]
	s_mov_b32 exec_hi, -1
	s_mov_b32 exec_lo, 0
	global_load_dwordx4 v[132:135], v149, s[18:19] offset:-512
	s_mov_b32 exec_lo, -1
	global_load_dwordx4 v[136:139], v150, s[8:9]
	global_load_dwordx4 v[140:143], v150, s[8:9] offset:256
	v_mov_b32_e32 v75, 0
	v_mov_b32_e32 v79, 0
	v_mov_b32_e32 v83, 0
	s_waitcnt vmcnt(22)
	v_mfma_f32_16x16x32_fp8_fp8 v[160:163], v[50:51], v[64:65], v[34:37]
	v_mfma_f32_16x16x32_fp8_fp8 v[164:167], v[52:53], v[64:65], v[22:25]
	s_waitcnt vmcnt(21)
	v_mfma_f32_16x16x32_fp8_fp8 v[168:171], v[46:47], v[64:65], v[38:41]
	v_mfma_f32_16x16x32_fp8_fp8 v[172:175], v[48:49], v[64:65], v[42:45]
	s_nop 3
	v_max3_f32 v86, v160, v161, v162
	v_max3_f32 v87, v163, v164, v165
	v_max3_f32 v88, v166, v167, v168
	v_max3_f32 v89, v169, v170, v171
	v_max3_f32 v86, v86, v172, v173
	v_max3_f32 v87, v87, v88, v89
	v_max_f32_e32 v96, v86, v87
	v_mul_f32_e32 v98, 0xbdb8aa3b, v96
	v_pk_fma_f32 v[208:209], v[160:161], s[30:31], v[98:99] op_sel_hi:[1,1,0]
	v_pk_fma_f32 v[210:211], v[162:163], s[30:31], v[98:99] op_sel_hi:[1,1,0]
	v_pk_fma_f32 v[212:213], v[164:165], s[30:31], v[98:99] op_sel_hi:[1,1,0]
	v_pk_fma_f32 v[214:215], v[166:167], s[30:31], v[98:99] op_sel_hi:[1,1,0]
	v_pk_fma_f32 v[216:217], v[168:169], s[30:31], v[98:99] op_sel_hi:[1,1,0]
	v_pk_fma_f32 v[218:219], v[170:171], s[30:31], v[98:99] op_sel_hi:[1,1,0]
	v_pk_fma_f32 v[220:221], v[172:173], s[30:31], v[98:99] op_sel_hi:[1,1,0]
	v_exp_f32_e32 v208, v208
	v_exp_f32_e32 v209, v209
	v_exp_f32_e32 v210, v210
	v_exp_f32_e32 v211, v211
	v_exp_f32_e32 v212, v212
	v_exp_f32_e32 v213, v213
	v_exp_f32_e32 v214, v214
	v_exp_f32_e32 v215, v215
	v_exp_f32_e32 v216, v216
	v_exp_f32_e32 v217, v217
	v_exp_f32_e32 v218, v218
	v_exp_f32_e32 v219, v219
	v_exp_f32_e32 v220, v220
	v_exp_f32_e32 v221, v221
	s_waitcnt vmcnt(20)
	v_mfma_f32_16x16x32_fp8_fp8 v[176:179], v[14:15], v[64:65], v[34:37]
	v_mfma_f32_16x16x32_fp8_fp8 v[180:183], v[16:17], v[64:65], v[22:25]
	s_waitcnt vmcnt(19)
	v_mfma_f32_16x16x32_fp8_fp8 v[184:187], v[10:11], v[64:65], v[38:41]
	v_mfma_f32_16x16x32_fp8_fp8 v[188:191], v[12:13], v[64:65], v[42:45]
	v_pk_add_f32 v[86:87], v[208:209], v[210:211]
	v_pk_add_f32 v[88:89], v[212:213], v[214:215]
	v_pk_add_f32 v[90:91], v[216:217], v[218:219]
	v_pk_mul_f32 v[92:93], v[208:209], v[160:161]
	v_pk_mul_f32 v[94:95], v[210:211], v[162:163]
	v_pk_add_f32 v[86:87], v[86:87], v[220:221]
	v_pk_add_f32 v[88:89], v[88:89], v[90:91]
	v_pk_fma_f32 v[92:93], v[212:213], v[164:165], v[92:93]
	v_pk_fma_f32 v[94:95], v[214:215], v[166:167], v[94:95]
	v_pk_add_f32 v[86:87], v[86:87], v[88:89]
	v_pk_fma_f32 v[92:93], v[216:217], v[168:169], v[92:93]
	v_pk_fma_f32 v[94:95], v[218:219], v[170:171], v[94:95]
	v_add_f32_e32 v86, v86, v87
	v_pk_fma_f32 v[92:93], v[220:221], v[172:173], v[92:93]
	v_rcp_f32_e32 v87, v86
	v_pk_add_f32 v[92:93], v[92:93], v[94:95]
	v_mul_f32_e32 v87, v55, v87
	v_add_f32_e32 v92, v92, v93
	v_mul_f32_e32 v107, v86, v87
	v_mul_f32_e32 v92, v92, v87
	v_mul_f32_e32 v100, 0x43800000, v87
	v_mul_f32_e32 v103, 0x3d800000, v92
	v_max3_f32 v86, v176, v177, v178
	v_max3_f32 v87, v179, v180, v181
	v_max3_f32 v88, v182, v183, v184
	v_max3_f32 v89, v185, v186, v187
	v_max3_f32 v86, v86, v188, v189
	v_max3_f32 v87, v87, v88, v89
	v_max_f32_e32 v96, v86, v87
	v_mul_f32_e32 v98, 0xbdb8aa3b, v96
	v_pk_fma_f32 v[222:223], v[176:177], s[30:31], v[98:99] op_sel_hi:[1,1,0]
	v_pk_fma_f32 v[224:225], v[178:179], s[30:31], v[98:99] op_sel_hi:[1,1,0]
	v_pk_fma_f32 v[226:227], v[180:181], s[30:31], v[98:99] op_sel_hi:[1,1,0]
	v_pk_fma_f32 v[228:229], v[182:183], s[30:31], v[98:99] op_sel_hi:[1,1,0]
	v_pk_fma_f32 v[230:231], v[184:185], s[30:31], v[98:99] op_sel_hi:[1,1,0]
	v_pk_fma_f32 v[232:233], v[186:187], s[30:31], v[98:99] op_sel_hi:[1,1,0]
	v_pk_fma_f32 v[234:235], v[188:189], s[30:31], v[98:99] op_sel_hi:[1,1,0]
	v_exp_f32_e32 v222, v222
	v_exp_f32_e32 v223, v223
	v_exp_f32_e32 v224, v224
	v_exp_f32_e32 v225, v225
	v_exp_f32_e32 v226, v226
	v_exp_f32_e32 v227, v227
	v_exp_f32_e32 v228, v228
	v_exp_f32_e32 v229, v229
	v_exp_f32_e32 v230, v230
	v_exp_f32_e32 v231, v231
	v_exp_f32_e32 v232, v232
	v_exp_f32_e32 v233, v233
	v_exp_f32_e32 v234, v234
	v_exp_f32_e32 v235, v235
	s_waitcnt vmcnt(18)
	v_mfma_f32_16x16x32_fp8_fp8 v[192:195], v[6:7], v[64:65], v[34:37]
	v_mfma_f32_16x16x32_fp8_fp8 v[196:199], v[8:9], v[64:65], v[22:25]
	s_waitcnt vmcnt(17)
	v_mfma_f32_16x16x32_fp8_fp8 v[200:203], v[2:3], v[64:65], v[38:41]
	v_mfma_f32_16x16x32_fp8_fp8 v[204:207], v[4:5], v[64:65], v[42:45]
	v_pk_add_f32 v[86:87], v[222:223], v[224:225]
	v_pk_add_f32 v[88:89], v[226:227], v[228:229]
	v_pk_add_f32 v[90:91], v[230:231], v[232:233]
	v_pk_mul_f32 v[92:93], v[222:223], v[176:177]
	v_pk_mul_f32 v[94:95], v[224:225], v[178:179]
	v_pk_add_f32 v[86:87], v[86:87], v[234:235]
	v_pk_add_f32 v[88:89], v[88:89], v[90:91]
	v_pk_fma_f32 v[92:93], v[226:227], v[180:181], v[92:93]
	v_pk_fma_f32 v[94:95], v[228:229], v[182:183], v[94:95]
	v_pk_add_f32 v[86:87], v[86:87], v[88:89]
	v_pk_fma_f32 v[92:93], v[230:231], v[184:185], v[92:93]
	v_pk_fma_f32 v[94:95], v[232:233], v[186:187], v[94:95]
	v_add_f32_e32 v86, v86, v87
	v_pk_fma_f32 v[92:93], v[234:235], v[188:189], v[92:93]
	v_rcp_f32_e32 v87, v86
	v_pk_add_f32 v[92:93], v[92:93], v[94:95]
	v_mul_f32_e32 v87, v55, v87
	v_add_f32_e32 v92, v92, v93
	v_mul_f32_e32 v108, v86, v87
	v_mul_f32_e32 v92, v92, v87
	v_mul_f32_e32 v101, 0x43800000, v87
	v_mul_f32_e32 v105, 0x3d800000, v92
	v_max3_f32 v86, v192, v193, v194
	v_max3_f32 v87, v195, v196, v197
	v_max3_f32 v88, v198, v199, v200
	v_max3_f32 v89, v201, v202, v203
	v_max3_f32 v86, v86, v204, v205
	v_max3_f32 v87, v87, v88, v89
	v_max_f32_e32 v96, v86, v87
	v_mul_f32_e32 v98, 0xbdb8aa3b, v96
	v_pk_fma_f32 v[236:237], v[192:193], s[30:31], v[98:99] op_sel_hi:[1,1,0]
	v_pk_fma_f32 v[238:239], v[194:195], s[30:31], v[98:99] op_sel_hi:[1,1,0]
	v_pk_fma_f32 v[240:241], v[196:197], s[30:31], v[98:99] op_sel_hi:[1,1,0]
	v_pk_fma_f32 v[242:243], v[198:199], s[30:31], v[98:99] op_sel_hi:[1,1,0]
	v_pk_fma_f32 v[244:245], v[200:201], s[30:31], v[98:99] op_sel_hi:[1,1,0]
	v_pk_fma_f32 v[246:247], v[202:203], s[30:31], v[98:99] op_sel_hi:[1,1,0]
	v_pk_fma_f32 v[248:249], v[204:205], s[30:31], v[98:99] op_sel_hi:[1,1,0]
	v_exp_f32_e32 v236, v236
	v_exp_f32_e32 v237, v237
	v_exp_f32_e32 v238, v238
	v_exp_f32_e32 v239, v239
	v_exp_f32_e32 v240, v240
	v_exp_f32_e32 v241, v241
	v_exp_f32_e32 v242, v242
	v_exp_f32_e32 v243, v243
	v_exp_f32_e32 v244, v244
	v_exp_f32_e32 v245, v245
	v_exp_f32_e32 v246, v246
	v_exp_f32_e32 v247, v247
	v_exp_f32_e32 v248, v248
	v_exp_f32_e32 v249, v249
	v_pk_add_f32 v[86:87], v[236:237], v[238:239]
	v_pk_add_f32 v[88:89], v[240:241], v[242:243]
	v_pk_add_f32 v[90:91], v[244:245], v[246:247]
	v_pk_mul_f32 v[92:93], v[236:237], v[192:193]
	v_pk_mul_f32 v[94:95], v[238:239], v[194:195]
	v_pk_add_f32 v[86:87], v[86:87], v[248:249]
	v_pk_add_f32 v[88:89], v[88:89], v[90:91]
	v_pk_fma_f32 v[92:93], v[240:241], v[196:197], v[92:93]
	v_pk_fma_f32 v[94:95], v[242:243], v[198:199], v[94:95]
	v_pk_add_f32 v[86:87], v[86:87], v[88:89]
	v_pk_fma_f32 v[92:93], v[244:245], v[200:201], v[92:93]
	v_pk_fma_f32 v[94:95], v[246:247], v[202:203], v[94:95]
	v_add_f32_e32 v86, v86, v87
	v_pk_fma_f32 v[92:93], v[248:249], v[204:205], v[92:93]
	v_rcp_f32_e32 v87, v86
	v_pk_add_f32 v[92:93], v[92:93], v[94:95]
	v_mul_f32_e32 v87, v55, v87
	v_add_f32_e32 v92, v92, v93
	v_mul_f32_e32 v109, v86, v87
	v_mul_f32_e32 v92, v92, v87
	v_mul_f32_e32 v102, 0x43800000, v87
	v_mul_f32_e32 v106, 0x3d800000, v92
	v_max3_f32 v122, v103, v105, v106
	v_cmp_gt_u32_e64 s[6:7], 16, v104
	v_mov_b32_e32 v123, v122
	s_nop 1
	v_permlane16_swap_b32_e32 v122, v123
	v_max_f32_e32 v122, v122, v123
	v_mov_b32_e32 v123, v122
	s_nop 1
	v_permlane32_swap_b32_e32 v122, v123
	v_max_f32_e32 v36, v122, v123
	v_mul_f32_e32 v123, 0x3fb8aa3b, v36
	v_fma_f32 v111, v103, v121, -v123
	v_exp_f32_e32 v111, v111
	s_nop 0
	v_mul_f32_e32 v112, v111, v100
	v_mul_f32_e32 v110, v111, v107
	v_mov_b32_e32 v114, v111
	v_pk_mul_f32 v[208:209], v[208:209], v[112:113] op_sel_hi:[1,0]
	v_pk_mul_f32 v[210:211], v[210:211], v[112:113] op_sel_hi:[1,0]
	v_pk_mul_f32 v[212:213], v[212:213], v[112:113] op_sel_hi:[1,0]
	v_pk_mul_f32 v[214:215], v[214:215], v[112:113] op_sel_hi:[1,0]
	v_pk_mul_f32 v[216:217], v[216:217], v[112:113] op_sel_hi:[1,0]
	v_pk_mul_f32 v[218:219], v[218:219], v[112:113] op_sel_hi:[1,0]
	v_pk_mul_f32 v[220:221], v[220:221], v[112:113] op_sel_hi:[1,0]
	s_waitcnt vmcnt(15)
	v_mov_b32_e32 v115, v110
	v_fma_mix_f32 v116, v110, v70, 0 op_sel_hi:[0,1,0]
	v_fma_mix_f32 v117, v110, v70, 0 op_sel:[0,1,0] op_sel_hi:[0,1,0]
	v_fma_mix_f32 v118, v110, v71, 0 op_sel_hi:[0,1,0]
	v_cvt_pk_fp8_f32 v72, v208, v209
	v_cvt_pk_fp8_f32 v73, v212, v213
	v_cvt_pk_fp8_f32 v74, v216, v217
	v_cvt_pk_fp8_f32 v75, v220, v221
	v_cvt_pk_fp8_f32 v72, v210, v211 op_sel:[0,0,1]
	v_cvt_pk_fp8_f32 v73, v214, v215 op_sel:[0,0,1]
	v_cvt_pk_fp8_f32 v74, v218, v219 op_sel:[0,0,1]
	s_nop 1
	v_mfma_f32_16x16x32_fp8_fp8 v[152:155], v[72:73], v[30:31], 0
	v_mfma_f32_16x16x32_fp8_fp8 v[152:155], v[74:75], v[32:33], v[152:155]
	v_fma_f32 v111, v105, v121, -v123
	v_exp_f32_e32 v111, v111
	s_nop 0
	v_mul_f32_e32 v112, v111, v101
	v_mul_f32_e32 v110, v111, v108
	v_add_f32_e32 v114, v114, v111
	v_pk_mul_f32 v[222:223], v[222:223], v[112:113] op_sel_hi:[1,0]
	v_pk_mul_f32 v[224:225], v[224:225], v[112:113] op_sel_hi:[1,0]
	v_pk_mul_f32 v[226:227], v[226:227], v[112:113] op_sel_hi:[1,0]
	v_pk_mul_f32 v[228:229], v[228:229], v[112:113] op_sel_hi:[1,0]
	v_pk_mul_f32 v[230:231], v[230:231], v[112:113] op_sel_hi:[1,0]
	v_pk_mul_f32 v[232:233], v[232:233], v[112:113] op_sel_hi:[1,0]
	v_pk_mul_f32 v[234:235], v[234:235], v[112:113] op_sel_hi:[1,0]
	s_waitcnt vmcnt(13)
	v_add_f32_e32 v115, v115, v110
	v_fma_mix_f32 v116, v110, v66, v116 op_sel_hi:[0,1,0]
	v_fma_mix_f32 v117, v110, v66, v117 op_sel:[0,1,0] op_sel_hi:[0,1,0]
	v_fma_mix_f32 v118, v110, v67, v118 op_sel_hi:[0,1,0]
	v_cvt_pk_fp8_f32 v76, v222, v223
	v_cvt_pk_fp8_f32 v77, v226, v227
	v_cvt_pk_fp8_f32 v78, v230, v231
	v_cvt_pk_fp8_f32 v79, v234, v235
	v_cvt_pk_fp8_f32 v76, v224, v225 op_sel:[0,0,1]
	v_cvt_pk_fp8_f32 v77, v228, v229 op_sel:[0,0,1]
	v_cvt_pk_fp8_f32 v78, v232, v233 op_sel:[0,0,1]
	s_nop 1
	v_mfma_f32_16x16x32_fp8_fp8 v[152:155], v[76:77], v[26:27], v[152:155]
	v_mfma_f32_16x16x32_fp8_fp8 v[152:155], v[78:79], v[28:29], v[152:155]
	v_fma_f32 v111, v106, v121, -v123
	v_exp_f32_e32 v111, v111
	s_nop 0
	v_mul_f32_e32 v112, v111, v102
	v_mul_f32_e32 v110, v111, v109
	v_add_f32_e32 v114, v114, v111
	v_pk_mul_f32 v[236:237], v[236:237], v[112:113] op_sel_hi:[1,0]
	v_pk_mul_f32 v[238:239], v[238:239], v[112:113] op_sel_hi:[1,0]
	v_pk_mul_f32 v[240:241], v[240:241], v[112:113] op_sel_hi:[1,0]
	v_pk_mul_f32 v[242:243], v[242:243], v[112:113] op_sel_hi:[1,0]
	v_pk_mul_f32 v[244:245], v[244:245], v[112:113] op_sel_hi:[1,0]
	v_pk_mul_f32 v[246:247], v[246:247], v[112:113] op_sel_hi:[1,0]
	v_pk_mul_f32 v[248:249], v[248:249], v[112:113] op_sel_hi:[1,0]
	s_waitcnt vmcnt(11)
	v_add_f32_e32 v115, v115, v110
	v_fma_mix_f32 v116, v110, v68, v116 op_sel_hi:[0,1,0]
	v_fma_mix_f32 v117, v110, v68, v117 op_sel:[0,1,0] op_sel_hi:[0,1,0]
	v_fma_mix_f32 v118, v110, v69, v118 op_sel_hi:[0,1,0]
	v_cvt_pk_fp8_f32 v80, v236, v237
	v_cvt_pk_fp8_f32 v81, v240, v241
	v_cvt_pk_fp8_f32 v82, v244, v245
	v_cvt_pk_fp8_f32 v83, v248, v249
	v_cvt_pk_fp8_f32 v80, v238, v239 op_sel:[0,0,1]
	v_cvt_pk_fp8_f32 v81, v242, v243 op_sel:[0,0,1]
	v_cvt_pk_fp8_f32 v82, v246, v247 op_sel:[0,0,1]
	s_nop 1
	v_mfma_f32_16x16x32_fp8_fp8 v[152:155], v[80:81], v[18:19], v[152:155]
	v_mfma_f32_16x16x32_fp8_fp8 v[152:155], v[82:83], v[20:21], v[152:155]
	v_mov_b32_e32 v86, v114
	v_mov_b32_e32 v87, v115
	v_mov_b32_e32 v88, v116
	v_mov_b32_e32 v89, v117
	v_mov_b32_e32 v90, v118
	v_permlane16_swap_b32_e32 v114, v86
	v_permlane16_swap_b32_e32 v115, v87
	v_permlane16_swap_b32_e32 v116, v88
	v_permlane16_swap_b32_e32 v117, v89
	v_permlane16_swap_b32_e32 v118, v90
	v_add_f32_e32 v114, v114, v86
	v_add_f32_e32 v115, v115, v87
	v_add_f32_e32 v116, v116, v88
	v_add_f32_e32 v117, v117, v89
	v_add_f32_e32 v118, v118, v90
	v_mov_b32_e32 v86, v114
	v_mov_b32_e32 v87, v115
	v_mov_b32_e32 v88, v116
	v_mov_b32_e32 v89, v117
	v_mov_b32_e32 v90, v118
	v_permlane32_swap_b32_e32 v114, v86
	v_permlane32_swap_b32_e32 v115, v87
	v_permlane32_swap_b32_e32 v116, v88
	v_permlane32_swap_b32_e32 v117, v89
	v_permlane32_swap_b32_e32 v118, v90
	v_add_f32_e32 v37, v114, v86
	v_add_f32_e32 v20, v115, v87
	v_add_f32_e32 v18, v116, v88
	v_add_f32_e32 v19, v117, v89
	v_add_f32_e32 v21, v118, v90
	ds_write2_b32 v156, v152, v153 offset0:0 offset1:20
	ds_write2_b32 v156, v154, v155 offset0:40 offset1:60
	s_branch .LBB1_30
.LBB1_16:
	global_load_dword v120, v144, s[12:13]
	global_load_dword v151, v144, s[14:15]
	global_load_dword v97, v145, s[10:11]
	global_load_dword v99, v145, s[10:11] offset:12
	global_load_dword v113, v145, s[10:11] offset:24
	global_load_dwordx4 v[124:127], v147, s[22:23]
	global_load_dwordx4 v[128:131], v148, s[22:23]
	s_mov_b32 exec_hi, 0
	global_load_dwordx4 v[132:135], v149, s[16:17]
	s_mov_b32 exec_hi, -1
	s_mov_b32 exec_lo, 0
	global_load_dwordx4 v[132:135], v149, s[18:19] offset:-512
	s_mov_b32 exec_lo, -1
	global_load_dwordx4 v[136:139], v150, s[8:9]
	global_load_dwordx4 v[140:143], v150, s[8:9] offset:256
	v_mov_b32_e32 v21, 0
	ds_write2_b32 v156, v21, v21 offset1:20
	ds_write2_b32 v156, v21, v21 offset0:40 offset1:60
	v_cmp_gt_u32_e64 s[6:7], 16, v104
	v_mov_b32_e32 v37, 1.0
	v_mov_b32_e32 v20, 0
	v_mov_b32_e32 v19, 0
	v_mov_b32_e32 v18, 0
	v_mov_b32_e32 v36, 0

.LBB1_32:
	s_or_b64 exec, exec, s[8:9]
	s_movk_i32 s6, 0x100
	v_cmp_gt_u32_e64 s[6:7], s6, v0
	s_waitcnt lgkmcnt(0)
	s_barrier
	s_and_saveexec_b64 s[14:15], s[6:7]
	s_cbranch_execz .LBB1_39
	ds_read_b96 v[160:162], v157 offset:12288
	ds_read_b96 v[164:166], v157 offset:12800
	ds_read_b96 v[168:170], v157 offset:13312
	ds_read_b96 v[172:174], v157 offset:13824
	ds_read2st64_b32 v[176:177], v158 offset0:48 offset1:50
	ds_read2st64_b32 v[178:179], v158 offset0:52 offset1:54
	ds_read2st64_b32 v[180:181], v159 offset0:28 offset1:33
	ds_read2st64_b32 v[182:183], v159 offset0:38 offset1:43
	v_cmp_gt_u32_e32 vcc, 3, v57
	v_cndmask_b32_e64 v18, 1.0, 0, s[20:21]
	s_waitcnt lgkmcnt(4)
	v_max_f32_e32 v21, v160, v164
	v_max3_f32 v33, v21, v168, v172
	v_sub_f32_e32 v21, v160, v33
	v_sub_f32_e32 v29, v164, v33
	v_sub_f32_e32 v30, v168, v33
	v_sub_f32_e32 v33, v172, v33
	v_mul_f32_e32 v21, 0x3fb8aa3b, v21
	v_mul_f32_e32 v29, 0x3fb8aa3b, v29
	v_mul_f32_e32 v30, 0x3fb8aa3b, v30
	v_mul_f32_e32 v33, 0x3fb8aa3b, v33
	v_exp_f32_e32 v21, v21
	v_exp_f32_e32 v29, v29
	v_exp_f32_e32 v30, v30
	v_exp_f32_e32 v33, v33
	v_mov_b32_e32 v20, v250
	v_mul_f32_e32 v35, v21, v161
	v_mul_f32_e32 v34, v21, v162
	v_fmac_f32_e32 v35, v29, v165
	v_fmac_f32_e32 v34, v29, v166
	v_fmac_f32_e32 v35, v30, v169
	v_fmac_f32_e32 v34, v30, v170
	v_fmac_f32_e32 v35, v33, v173
	v_fmac_f32_e32 v34, v33, v174
	v_rcp_f32_e32 v35, v35
	s_waitcnt lgkmcnt(0)
	v_mul_f32_e32 v31, v21, v180
	v_mul_f32_e32 v18, v18, v35
	v_fmac_f32_e32 v31, v29, v181
	v_mul_f32_e32 v35, v21, v176
	v_fmac_f32_e32 v31, v30, v182
	v_fmac_f32_e32 v35, v29, v177
	v_fmac_f32_e32 v31, v33, v183
	v_fmac_f32_e32 v35, v30, v178
	v_mul_f32_e32 v31, v31, v18
	v_fmac_f32_e32 v35, v33, v179
	s_mov_b32 s8, 0x3a800000
	v_fma_mixlo_f16 v31, v31, s8, 0
	v_cmp_eq_u32_e64 s[8:9], 7, v57
	s_and_saveexec_b64 s[10:11], s[4:5]
	ds_write_b16 v251, v31
	s_and_b64 exec, exec, s[8:9]
	v_mov_b32_e32 v31, 0x3c00
	ds_write_b16 v20, v31 offset:46
	s_or_b64 exec, exec, s[10:11]
	s_waitcnt vmcnt(6)
	v_fma_f32 v33, v34, v151, -v35
	v_cmp_eq_u32_e64 s[8:9], 0, v57
	v_fma_f32 v32, v18, v33, -v120
	s_and_b64 s[12:13], vcc, s[4:5]
	s_nop 0
	v_mov_b32_dpp v26, v32 quad_perm:[0,0,0,0] row_mask:0xf bank_mask:0xf bound_ctrl:1
	v_mov_b32_dpp v27, v32 quad_perm:[1,1,1,1] row_mask:0xf bank_mask:0xf bound_ctrl:1
	v_mov_b32_dpp v28, v32 quad_perm:[2,2,2,2] row_mask:0xf bank_mask:0xf bound_ctrl:1
	s_and_b64 exec, exec, s[12:13]
	s_cbranch_execz .LBB1_39
	v_mul_f32_e32 v20, v97, v26
	v_fmac_f32_e32 v20, v99, v27
	v_fmac_f32_e32 v20, v113, v28
	v_mul_f32_e32 v30, v20, v20
	v_cvt_f16_f32_e32 v27, v20
	s_nop 0
	v_mov_b32_dpp v31, v30 quad_perm:[1,2,0,3] row_mask:0xf bank_mask:0xf bound_ctrl:1
	v_mov_b32_dpp v19, v30 quad_perm:[2,0,1,3] row_mask:0xf bank_mask:0xf bound_ctrl:1
	ds_write_b16 v61, v27 offset:14368
	v_add_f32_e32 v18, v30, v31
	v_add_f32_e32 v18, v18, v19
	v_sqrt_f32_e32 v18, v18
	s_nop 0
	v_add_f32_e32 v21, 0x38d1b717, v18
	v_rcp_f32_e32 v21, v21
	s_nop 0
	v_fma_mixlo_f16 v20, v20, v21, 0
	ds_write_b16 v62, v20 offset:14368
	s_and_b64 exec, exec, s[8:9]
	s_cbranch_execz .LBB1_39
	v_cvt_f16_f32_e32 v18, v18
	ds_write_b16 v119, v18 offset:14848
